# v40 but the NMT=1 (second-pass) P2a loops prefetch deeper: A gather 2 steps ahead + W loads at groups 4..7; first-pass loops unchanged
# baseline (speedup 1.0000x reference)
.LBB0_283:
	s_cmp_lt_u32 s50, 13
	s_cselect_b64 vcc, -1, 0
	s_min_u32 s6, s50, 12
	s_lshl_b32 s6, s6, 17
	s_add_u32 s51, s22, s6
	s_waitcnt vmcnt(6)
	s_addc_u32 s52, s23, 0
	ds_read_b128 v[50:53], v172
	ds_read_b64_tr_b16 v[54:55], v171
	ds_read_b64_tr_b16 v[56:57], v171 offset:1024
	s_add_u32 s6, s51, 0x60000
	ds_read_b64_tr_b16 v[58:59], v179
	ds_read_b64_tr_b16 v[60:61], v179 offset:1024
	s_addc_u32 s7, s52, 0
	s_add_u32 s10, s8, 0x100
	s_min_u32 s10, s10, 0x780
	s_add_u32 s10, s18, s10
	v_cvt_pk_bf16_f32 v18, v18, v19
	v_cvt_pk_bf16_f32 v19, v20, v21
	v_cndmask_b32_e32 v49, 0, v168, vcc
	s_addc_u32 s11, s19, 0
	s_waitcnt lgkmcnt(2)
	v_mfma_f32_16x16x32_bf16 v[54:57], v[54:57], v[50:53], v[94:97]
	ds_write_b64 v186, v[18:19] offset:16384
	ds_read_b64_tr_b16 v[244:245], v180
	ds_read_b64_tr_b16 v[246:247], v180 offset:1024
	v_cvt_pk_bf16_f32 v6, v6, v7
	v_cvt_pk_bf16_f32 v7, v8, v9
	s_waitcnt lgkmcnt(3)
	v_mfma_f32_16x16x32_bf16 v[58:61], v[58:61], v[50:53], v[90:93]
	ds_write_b64 v46, v[6:7] offset:16640
	ds_read_b64_tr_b16 v[248:249], v181
	ds_read_b64_tr_b16 v[250:251], v181 offset:1024
	s_waitcnt lgkmcnt(3)
	v_mfma_f32_16x16x32_bf16 v[244:247], v[244:247], v[50:53], v[70:73]
	v_cvt_pk_bf16_f32 v14, v14, v15
	v_cvt_pk_bf16_f32 v15, v16, v17
	ds_write_b64 v47, v[14:15] offset:16896
	ds_read_b64_tr_b16 v[240:241], v182
	ds_read_b64_tr_b16 v[242:243], v182 offset:1024
	s_waitcnt lgkmcnt(3)
	v_mfma_f32_16x16x32_bf16 v[248:251], v[248:251], v[50:53], v[42:45]
	v_cvt_pk_bf16_f32 v2, v2, v3
	v_cvt_pk_bf16_f32 v3, v4, v5
	ds_write_b64 v48, v[2:3] offset:17152
	ds_read_b64_tr_b16 v[236:237], v183
	ds_read_b64_tr_b16 v[238:239], v183 offset:1024
	s_waitcnt lgkmcnt(3)
	v_mfma_f32_16x16x32_bf16 v[240:243], v[240:243], v[50:53], v[86:89]
	global_load_dwordx4 v[18:21], v49, s[6:7]
	ds_read_b64_tr_b16 v[42:43], v184
	ds_read_b64_tr_b16 v[44:45], v184 offset:1024
	s_waitcnt lgkmcnt(2)
	v_mfma_f32_16x16x32_bf16 v[236:239], v[236:239], v[50:53], v[62:65]
	global_load_dwordx4 v[6:9], v49, s[6:7] offset:2048
	s_nop 2
	ds_read_b64_tr_b16 v[62:63], v185
	ds_read_b64_tr_b16 v[64:65], v185 offset:1024
	s_waitcnt lgkmcnt(2)
	v_mfma_f32_16x16x32_bf16 v[30:33], v[42:45], v[50:53], v[30:33]
	s_add_u32 s6, s51, 0x61000
	s_addc_u32 s7, s52, 0
	global_load_dwordx4 v[14:17], v49, s[6:7]
	ds_read_b64_tr_b16 v[42:43], v171 offset:8192
	ds_read_b64_tr_b16 v[44:45], v171 offset:9216
	ds_read_b128 v[66:69], v178
	s_waitcnt lgkmcnt(3)
	v_mfma_f32_16x16x32_bf16 v[10:13], v[62:65], v[50:53], v[10:13]
	global_load_dwordx4 v[2:5], v49, s[6:7] offset:2048
	ds_read_b64_tr_b16 v[50:51], v179 offset:8192
	ds_read_b64_tr_b16 v[52:53], v179 offset:9216
	s_waitcnt lgkmcnt(2)
	v_mfma_f32_16x16x32_bf16 v[42:45], v[42:45], v[66:69], v[54:57]
	s_mov_b32 s53, m0
	s_mov_b32 m0, s67
	s_nop 0
	global_load_lds_dwordx4 v169, s[10:11]
	s_mov_b32 m0, s53
	s_nop 2
	ds_read_b64_tr_b16 v[54:55], v180 offset:8192
	ds_read_b64_tr_b16 v[56:57], v180 offset:9216
	s_waitcnt lgkmcnt(2)
	v_mfma_f32_16x16x32_bf16 v[50:53], v[50:53], v[66:69], v[58:61]
	s_mov_b32 s53, m0
	s_mov_b32 m0, s68
	s_nop 0
	global_load_lds_dwordx4 v170, s[10:11]
	s_mov_b32 m0, s53
	s_nop 2
	ds_read_b64_tr_b16 v[58:59], v181 offset:8192
	ds_read_b64_tr_b16 v[60:61], v181 offset:9216
	s_waitcnt lgkmcnt(2)
	v_mfma_f32_16x16x32_bf16 v[54:57], v[54:57], v[66:69], v[244:247]
	s_nop 2
	ds_read_b64_tr_b16 v[244:245], v182 offset:8192
	ds_read_b64_tr_b16 v[246:247], v182 offset:9216
	s_waitcnt lgkmcnt(2)
	v_mfma_f32_16x16x32_bf16 v[58:61], v[58:61], v[66:69], v[248:251]
	s_nop 2
	ds_read_b64_tr_b16 v[248:249], v183 offset:8192
	ds_read_b64_tr_b16 v[250:251], v183 offset:9216
	s_waitcnt lgkmcnt(2)
	v_mfma_f32_16x16x32_bf16 v[62:65], v[244:247], v[66:69], v[240:243]
	s_nop 2
	ds_read_b64_tr_b16 v[240:241], v184 offset:8192
	ds_read_b64_tr_b16 v[242:243], v184 offset:9216
	s_waitcnt lgkmcnt(2)
	v_mfma_f32_16x16x32_bf16 v[70:73], v[248:251], v[66:69], v[236:239]
	ds_read_b64_tr_b16 v[74:75], v185 offset:8192
	ds_read_b64_tr_b16 v[76:77], v185 offset:9216
	s_waitcnt lgkmcnt(2)
	v_mfma_f32_16x16x32_bf16 v[30:33], v[240:243], v[66:69], v[30:33]
	s_waitcnt lgkmcnt(0)
	v_mfma_f32_16x16x32_bf16 v[10:13], v[74:77], v[66:69], v[10:13]
	s_add_i32 s51, s50, 2
	s_cmp_lt_u32 s50, 12
	s_cselect_b64 vcc, -1, 0
	s_min_u32 s6, s50, 11
	s_lshl_b32 s6, s6, 17
	s_waitcnt lgkmcnt(0)
	s_barrier
	s_add_u32 s69, s22, s6
	s_waitcnt vmcnt(6)
	s_addc_u32 s70, s23, 0
	s_add_u32 s10, s69, 0x80000
	ds_read_b64_tr_b16 v[66:67], v171 offset:16384
	ds_read_b64_tr_b16 v[68:69], v171 offset:17408
	ds_read_b128 v[74:77], v172 offset:8192
	s_addc_u32 s11, s70, 0
	s_add_u32 s8, s8, 0x100
	s_addc_u32 s9, s9, 0
	s_cmp_lt_u32 s50, 14
	ds_read_b64_tr_b16 v[78:79], v179 offset:16384
	ds_read_b64_tr_b16 v[80:81], v179 offset:17408
	s_cselect_b64 s[6:7], -1, 0
	s_waitcnt lgkmcnt(2)
	v_mfma_f32_16x16x32_bf16 v[42:45], v[66:69], v[74:77], v[42:45]
	v_cndmask_b32_e32 v49, 0, v168, vcc
	s_and_b64 vcc, s[6:7], exec
	s_add_i32 s50, s8, 0x80
	s_min_u32 s50, s50, 0x780
	s_add_u32 s52, s18, s50
	v_cvt_pk_bf16_f32 v38, v38, v39
	v_cvt_pk_bf16_f32 v39, v40, v41
	s_addc_u32 s53, s19, 0
	ds_write_b64 v186, v[38:39]
	ds_read_b64_tr_b16 v[244:245], v180 offset:16384
	ds_read_b64_tr_b16 v[246:247], v180 offset:17408
	v_cvt_pk_bf16_f32 v26, v26, v27
	v_cvt_pk_bf16_f32 v27, v28, v29
	s_waitcnt lgkmcnt(3)
	v_mfma_f32_16x16x32_bf16 v[50:53], v[78:81], v[74:77], v[50:53]
	ds_write_b64 v46, v[26:27] offset:256
	ds_read_b64_tr_b16 v[248:249], v181 offset:16384
	ds_read_b64_tr_b16 v[250:251], v181 offset:17408
	s_waitcnt lgkmcnt(3)
	v_mfma_f32_16x16x32_bf16 v[244:247], v[244:247], v[74:77], v[54:57]
	v_cvt_pk_bf16_f32 v34, v34, v35
	v_cvt_pk_bf16_f32 v35, v36, v37
	ds_write_b64 v47, v[34:35] offset:512
	ds_read_b64_tr_b16 v[240:241], v182 offset:16384
	ds_read_b64_tr_b16 v[242:243], v182 offset:17408
	s_waitcnt lgkmcnt(3)
	v_mfma_f32_16x16x32_bf16 v[248:251], v[248:251], v[74:77], v[58:61]
	v_cvt_pk_bf16_f32 v22, v22, v23
	v_cvt_pk_bf16_f32 v23, v24, v25
	ds_write_b64 v48, v[22:23] offset:768
	ds_read_b64_tr_b16 v[236:237], v183 offset:16384
	ds_read_b64_tr_b16 v[238:239], v183 offset:17408
	s_waitcnt lgkmcnt(3)
	v_mfma_f32_16x16x32_bf16 v[240:243], v[240:243], v[74:77], v[62:65]
	global_load_dwordx4 v[38:41], v49, s[10:11]
	ds_read_b64_tr_b16 v[54:55], v184 offset:16384
	ds_read_b64_tr_b16 v[56:57], v184 offset:17408
	s_waitcnt lgkmcnt(2)
	v_mfma_f32_16x16x32_bf16 v[236:239], v[236:239], v[74:77], v[70:73]
	global_load_dwordx4 v[26:29], v49, s[10:11] offset:2048
	ds_read_b64_tr_b16 v[58:59], v185 offset:16384
	ds_read_b64_tr_b16 v[60:61], v185 offset:17408
	s_waitcnt lgkmcnt(2)
	v_mfma_f32_16x16x32_bf16 v[30:33], v[54:57], v[74:77], v[30:33]
	s_add_u32 s6, s69, 0x81000
	s_addc_u32 s7, s70, 0
	global_load_dwordx4 v[34:37], v49, s[6:7]
	ds_read_b64_tr_b16 v[54:55], v171 offset:24576
	ds_read_b64_tr_b16 v[56:57], v171 offset:25600
	ds_read_b128 v[66:69], v187
	s_waitcnt lgkmcnt(3)
	v_mfma_f32_16x16x32_bf16 v[10:13], v[58:61], v[74:77], v[10:13]
	global_load_dwordx4 v[22:25], v49, s[6:7] offset:2048
	ds_read_b64_tr_b16 v[58:59], v179 offset:24576
	ds_read_b64_tr_b16 v[60:61], v179 offset:25600
	s_waitcnt lgkmcnt(2)
	v_mfma_f32_16x16x32_bf16 v[94:97], v[54:57], v[66:69], v[42:45]
	s_mov_b32 s50, m0
	s_mov_b32 m0, s48
	s_nop 0
	global_load_lds_dwordx4 v169, s[52:53]
	s_mov_b32 m0, s50
	s_nop 2
	ds_read_b64_tr_b16 v[42:43], v180 offset:24576
	ds_read_b64_tr_b16 v[44:45], v180 offset:25600
	s_waitcnt lgkmcnt(2)
	v_mfma_f32_16x16x32_bf16 v[90:93], v[58:61], v[66:69], v[50:53]
	s_mov_b32 s50, m0
	s_mov_b32 m0, s49
	s_nop 0
	global_load_lds_dwordx4 v170, s[52:53]
	s_mov_b32 m0, s50
	s_nop 2
	ds_read_b64_tr_b16 v[50:51], v181 offset:24576
	ds_read_b64_tr_b16 v[52:53], v181 offset:25600
	s_waitcnt lgkmcnt(2)
	v_mfma_f32_16x16x32_bf16 v[70:73], v[42:45], v[66:69], v[244:247]
	s_nop 2
	ds_read_b64_tr_b16 v[244:245], v182 offset:24576
	ds_read_b64_tr_b16 v[246:247], v182 offset:25600
	s_waitcnt lgkmcnt(2)
	v_mfma_f32_16x16x32_bf16 v[42:45], v[50:53], v[66:69], v[248:251]
	s_nop 2
	ds_read_b64_tr_b16 v[248:249], v183 offset:24576
	ds_read_b64_tr_b16 v[250:251], v183 offset:25600
	s_waitcnt lgkmcnt(2)
	v_mfma_f32_16x16x32_bf16 v[86:89], v[244:247], v[66:69], v[240:243]
	s_nop 2
	ds_read_b64_tr_b16 v[240:241], v184 offset:24576
	ds_read_b64_tr_b16 v[242:243], v184 offset:25600
	s_waitcnt lgkmcnt(2)
	v_mfma_f32_16x16x32_bf16 v[62:65], v[248:251], v[66:69], v[236:239]
	ds_read_b64_tr_b16 v[50:51], v185 offset:24576
	ds_read_b64_tr_b16 v[52:53], v185 offset:25600
	s_waitcnt lgkmcnt(2)
	v_mfma_f32_16x16x32_bf16 v[30:33], v[240:243], v[66:69], v[30:33]
	s_waitcnt lgkmcnt(0)
	v_mfma_f32_16x16x32_bf16 v[10:13], v[50:53], v[66:69], v[10:13]
	s_waitcnt lgkmcnt(0)
	s_barrier
	s_mov_b32 s50, s51
	s_cbranch_vccnz .LBB0_283
	s_waitcnt vmcnt(0)
	s_waitcnt lgkmcnt(0)
	s_barrier
	v_mov_b32_e32 v77, 0
	v_mov_b32_e32 v76, v77
	v_mov_b32_e32 v75, v77
	v_mov_b32_e32 v74, v77
	v_mov_b32_e32 v81, v77
	v_mov_b32_e32 v80, v77
	v_mov_b32_e32 v79, v77
	v_mov_b32_e32 v78, v77
	v_mov_b32_e32 v125, v77
	v_mov_b32_e32 v124, v77
	v_mov_b32_e32 v123, v77
	v_mov_b32_e32 v122, v77
	v_mov_b32_e32 v49, v77
	v_mov_b32_e32 v48, v77
	v_mov_b32_e32 v47, v77
	v_mov_b32_e32 v46, v77
	v_mov_b32_e32 v61, v77
	v_mov_b32_e32 v60, v77
	v_mov_b32_e32 v59, v77
	v_mov_b32_e32 v58, v77
	v_mov_b32_e32 v117, v77
	v_mov_b32_e32 v116, v77
	v_mov_b32_e32 v115, v77
	v_mov_b32_e32 v114, v77
	v_mov_b32_e32 v21, v77
	v_mov_b32_e32 v20, v77
	v_mov_b32_e32 v19, v77
	v_mov_b32_e32 v18, v77
	v_mov_b32_e32 v41, v77
	v_mov_b32_e32 v40, v77
	v_mov_b32_e32 v39, v77
	v_mov_b32_e32 v38, v77
	v_mov_b32_e32 v109, v77
	v_mov_b32_e32 v108, v77
	v_mov_b32_e32 v107, v77
	v_mov_b32_e32 v106, v77
	v_mov_b32_e32 v9, v77
	v_mov_b32_e32 v8, v77
	v_mov_b32_e32 v7, v77
	v_mov_b32_e32 v6, v77
	v_mov_b32_e32 v25, v77
	v_mov_b32_e32 v24, v77
	v_mov_b32_e32 v23, v77
	v_mov_b32_e32 v22, v77
	v_mov_b32_e32 v105, v77
	v_mov_b32_e32 v104, v77
	v_mov_b32_e32 v103, v77
	v_mov_b32_e32 v102, v77
	v_mov_b32_e32 v57, v77
	v_mov_b32_e32 v56, v77
	v_mov_b32_e32 v55, v77
	v_mov_b32_e32 v54, v77
	v_mov_b32_e32 v85, v77
	v_mov_b32_e32 v84, v77
	v_mov_b32_e32 v83, v77
	v_mov_b32_e32 v82, v77
	v_mov_b32_e32 v129, v77
	v_mov_b32_e32 v128, v77
	v_mov_b32_e32 v127, v77
	v_mov_b32_e32 v126, v77
	v_mov_b32_e32 v37, v77
	v_mov_b32_e32 v36, v77
	v_mov_b32_e32 v35, v77
	v_mov_b32_e32 v34, v77
	v_mov_b32_e32 v69, v77
	v_mov_b32_e32 v68, v77
	v_mov_b32_e32 v67, v77
	v_mov_b32_e32 v66, v77
	v_mov_b32_e32 v121, v77
	v_mov_b32_e32 v120, v77
	v_mov_b32_e32 v119, v77
	v_mov_b32_e32 v118, v77
	v_mov_b32_e32 v17, v77
	v_mov_b32_e32 v16, v77
	v_mov_b32_e32 v15, v77
	v_mov_b32_e32 v14, v77
	v_mov_b32_e32 v53, v77
	v_mov_b32_e32 v52, v77
	v_mov_b32_e32 v51, v77
	v_mov_b32_e32 v50, v77
	v_mov_b32_e32 v113, v77
	v_mov_b32_e32 v112, v77
	v_mov_b32_e32 v111, v77
	v_mov_b32_e32 v110, v77
	v_mov_b32_e32 v5, v77
	v_mov_b32_e32 v4, v77
	v_mov_b32_e32 v3, v77
	v_mov_b32_e32 v2, v77
	v_mov_b32_e32 v29, v77
	v_mov_b32_e32 v28, v77
	v_mov_b32_e32 v27, v77
	v_mov_b32_e32 v26, v77
	v_mov_b32_e32 v101, v77
	v_mov_b32_e32 v100, v77
	v_mov_b32_e32 v99, v77
	v_mov_b32_e32 v98, v77

.LBB0_889:
	s_cmp_lt_u32 s48, 13
	s_cselect_b64 vcc, -1, 0
	s_min_u32 s10, s48, 12
	s_lshl_b32 s10, s10, 17
	s_add_u32 s49, s22, s10
	s_waitcnt vmcnt(6)
	s_addc_u32 s50, s23, 0
	ds_read_b128 v[50:53], v172
	ds_read_b64_tr_b16 v[54:55], v171
	ds_read_b64_tr_b16 v[56:57], v171 offset:1024
	s_add_u32 s10, s49, 0x60000
	ds_read_b64_tr_b16 v[58:59], v179
	ds_read_b64_tr_b16 v[60:61], v179 offset:1024
	s_addc_u32 s11, s50, 0
	s_add_u32 s14, s12, 0x100
	s_min_u32 s14, s14, 0x780
	s_add_u32 s14, s8, s14
	v_cvt_pk_bf16_f32 v18, v18, v19
	v_cvt_pk_bf16_f32 v19, v20, v21
	v_cndmask_b32_e32 v49, 0, v168, vcc
	s_addc_u32 s15, s9, 0
	s_waitcnt lgkmcnt(2)
	v_mfma_f32_16x16x32_bf16 v[54:57], v[54:57], v[50:53], v[94:97]
	ds_write_b64 v186, v[18:19] offset:16384
	ds_read_b64_tr_b16 v[244:245], v180
	ds_read_b64_tr_b16 v[246:247], v180 offset:1024
	v_cvt_pk_bf16_f32 v6, v6, v7
	v_cvt_pk_bf16_f32 v7, v8, v9
	s_waitcnt lgkmcnt(3)
	v_mfma_f32_16x16x32_bf16 v[58:61], v[58:61], v[50:53], v[90:93]
	ds_write_b64 v46, v[6:7] offset:16640
	ds_read_b64_tr_b16 v[248:249], v181
	ds_read_b64_tr_b16 v[250:251], v181 offset:1024
	s_waitcnt lgkmcnt(3)
	v_mfma_f32_16x16x32_bf16 v[244:247], v[244:247], v[50:53], v[70:73]
	v_cvt_pk_bf16_f32 v14, v14, v15
	v_cvt_pk_bf16_f32 v15, v16, v17
	ds_write_b64 v47, v[14:15] offset:16896
	ds_read_b64_tr_b16 v[240:241], v182
	ds_read_b64_tr_b16 v[242:243], v182 offset:1024
	s_waitcnt lgkmcnt(3)
	v_mfma_f32_16x16x32_bf16 v[248:251], v[248:251], v[50:53], v[42:45]
	v_cvt_pk_bf16_f32 v2, v2, v3
	v_cvt_pk_bf16_f32 v3, v4, v5
	ds_write_b64 v48, v[2:3] offset:17152
	ds_read_b64_tr_b16 v[236:237], v183
	ds_read_b64_tr_b16 v[238:239], v183 offset:1024
	s_waitcnt lgkmcnt(3)
	v_mfma_f32_16x16x32_bf16 v[240:243], v[240:243], v[50:53], v[86:89]
	global_load_dwordx4 v[18:21], v49, s[10:11]
	ds_read_b64_tr_b16 v[42:43], v184
	ds_read_b64_tr_b16 v[44:45], v184 offset:1024
	s_waitcnt lgkmcnt(2)
	v_mfma_f32_16x16x32_bf16 v[236:239], v[236:239], v[50:53], v[62:65]
	global_load_dwordx4 v[6:9], v49, s[10:11] offset:2048
	s_nop 2
	ds_read_b64_tr_b16 v[62:63], v185
	ds_read_b64_tr_b16 v[64:65], v185 offset:1024
	s_waitcnt lgkmcnt(2)
	v_mfma_f32_16x16x32_bf16 v[30:33], v[42:45], v[50:53], v[30:33]
	s_add_u32 s10, s49, 0x61000
	s_addc_u32 s11, s50, 0
	global_load_dwordx4 v[14:17], v49, s[10:11]
	ds_read_b64_tr_b16 v[42:43], v171 offset:8192
	ds_read_b64_tr_b16 v[44:45], v171 offset:9216
	ds_read_b128 v[66:69], v178
	s_waitcnt lgkmcnt(3)
	v_mfma_f32_16x16x32_bf16 v[10:13], v[62:65], v[50:53], v[10:13]
	global_load_dwordx4 v[2:5], v49, s[10:11] offset:2048
	ds_read_b64_tr_b16 v[50:51], v179 offset:8192
	ds_read_b64_tr_b16 v[52:53], v179 offset:9216
	s_waitcnt lgkmcnt(2)
	v_mfma_f32_16x16x32_bf16 v[42:45], v[42:45], v[66:69], v[54:57]
	s_mov_b32 s51, m0
	s_mov_b32 m0, s67
	s_nop 0
	global_load_lds_dwordx4 v169, s[14:15]
	s_mov_b32 m0, s51
	s_nop 2
	ds_read_b64_tr_b16 v[54:55], v180 offset:8192
	ds_read_b64_tr_b16 v[56:57], v180 offset:9216
	s_waitcnt lgkmcnt(2)
	v_mfma_f32_16x16x32_bf16 v[50:53], v[50:53], v[66:69], v[58:61]
	s_mov_b32 s51, m0
	s_mov_b32 m0, s68
	s_nop 0
	global_load_lds_dwordx4 v170, s[14:15]
	s_mov_b32 m0, s51
	s_nop 2
	ds_read_b64_tr_b16 v[58:59], v181 offset:8192
	ds_read_b64_tr_b16 v[60:61], v181 offset:9216
	s_waitcnt lgkmcnt(2)
	v_mfma_f32_16x16x32_bf16 v[54:57], v[54:57], v[66:69], v[244:247]
	s_nop 2
	ds_read_b64_tr_b16 v[244:245], v182 offset:8192
	ds_read_b64_tr_b16 v[246:247], v182 offset:9216
	s_waitcnt lgkmcnt(2)
	v_mfma_f32_16x16x32_bf16 v[58:61], v[58:61], v[66:69], v[248:251]
	s_nop 2
	ds_read_b64_tr_b16 v[248:249], v183 offset:8192
	ds_read_b64_tr_b16 v[250:251], v183 offset:9216
	s_waitcnt lgkmcnt(2)
	v_mfma_f32_16x16x32_bf16 v[62:65], v[244:247], v[66:69], v[240:243]
	s_nop 2
	ds_read_b64_tr_b16 v[240:241], v184 offset:8192
	ds_read_b64_tr_b16 v[242:243], v184 offset:9216
	s_waitcnt lgkmcnt(2)
	v_mfma_f32_16x16x32_bf16 v[70:73], v[248:251], v[66:69], v[236:239]
	ds_read_b64_tr_b16 v[74:75], v185 offset:8192
	ds_read_b64_tr_b16 v[76:77], v185 offset:9216
	s_waitcnt lgkmcnt(2)
	v_mfma_f32_16x16x32_bf16 v[30:33], v[240:243], v[66:69], v[30:33]
	s_waitcnt lgkmcnt(0)
	v_mfma_f32_16x16x32_bf16 v[10:13], v[74:77], v[66:69], v[10:13]
	s_add_i32 s49, s48, 2
	s_cmp_lt_u32 s48, 12
	s_cselect_b64 vcc, -1, 0
	s_min_u32 s10, s48, 11
	s_lshl_b32 s10, s10, 17
	s_waitcnt lgkmcnt(0)
	s_barrier
	s_add_u32 s69, s22, s10
	s_waitcnt vmcnt(6)
	s_addc_u32 s70, s23, 0
	s_add_u32 s14, s69, 0x80000
	ds_read_b64_tr_b16 v[66:67], v171 offset:16384
	ds_read_b64_tr_b16 v[68:69], v171 offset:17408
	ds_read_b128 v[74:77], v172 offset:8192
	s_addc_u32 s15, s70, 0
	s_add_u32 s12, s12, 0x100
	s_addc_u32 s13, s13, 0
	s_cmp_lt_u32 s48, 14
	ds_read_b64_tr_b16 v[78:79], v179 offset:16384
	ds_read_b64_tr_b16 v[80:81], v179 offset:17408
	s_cselect_b64 s[10:11], -1, 0
	s_waitcnt lgkmcnt(2)
	v_mfma_f32_16x16x32_bf16 v[42:45], v[66:69], v[74:77], v[42:45]
	v_cndmask_b32_e32 v49, 0, v168, vcc
	s_and_b64 vcc, s[10:11], exec
	s_add_i32 s48, s12, 0x80
	s_min_u32 s48, s48, 0x780
	s_add_u32 s50, s8, s48
	v_cvt_pk_bf16_f32 v38, v38, v39
	v_cvt_pk_bf16_f32 v39, v40, v41
	s_addc_u32 s51, s9, 0
	ds_write_b64 v186, v[38:39]
	ds_read_b64_tr_b16 v[244:245], v180 offset:16384
	ds_read_b64_tr_b16 v[246:247], v180 offset:17408
	v_cvt_pk_bf16_f32 v26, v26, v27
	v_cvt_pk_bf16_f32 v27, v28, v29
	s_waitcnt lgkmcnt(3)
	v_mfma_f32_16x16x32_bf16 v[50:53], v[78:81], v[74:77], v[50:53]
	ds_write_b64 v46, v[26:27] offset:256
	ds_read_b64_tr_b16 v[248:249], v181 offset:16384
	ds_read_b64_tr_b16 v[250:251], v181 offset:17408
	s_waitcnt lgkmcnt(3)
	v_mfma_f32_16x16x32_bf16 v[244:247], v[244:247], v[74:77], v[54:57]
	v_cvt_pk_bf16_f32 v34, v34, v35
	v_cvt_pk_bf16_f32 v35, v36, v37
	ds_write_b64 v47, v[34:35] offset:512
	ds_read_b64_tr_b16 v[240:241], v182 offset:16384
	ds_read_b64_tr_b16 v[242:243], v182 offset:17408
	s_waitcnt lgkmcnt(3)
	v_mfma_f32_16x16x32_bf16 v[248:251], v[248:251], v[74:77], v[58:61]
	v_cvt_pk_bf16_f32 v22, v22, v23
	v_cvt_pk_bf16_f32 v23, v24, v25
	ds_write_b64 v48, v[22:23] offset:768
	ds_read_b64_tr_b16 v[236:237], v183 offset:16384
	ds_read_b64_tr_b16 v[238:239], v183 offset:17408
	s_waitcnt lgkmcnt(3)
	v_mfma_f32_16x16x32_bf16 v[240:243], v[240:243], v[74:77], v[62:65]
	global_load_dwordx4 v[38:41], v49, s[14:15]
	ds_read_b64_tr_b16 v[54:55], v184 offset:16384
	ds_read_b64_tr_b16 v[56:57], v184 offset:17408
	s_waitcnt lgkmcnt(2)
	v_mfma_f32_16x16x32_bf16 v[236:239], v[236:239], v[74:77], v[70:73]
	global_load_dwordx4 v[26:29], v49, s[14:15] offset:2048
	ds_read_b64_tr_b16 v[58:59], v185 offset:16384
	ds_read_b64_tr_b16 v[60:61], v185 offset:17408
	s_waitcnt lgkmcnt(2)
	v_mfma_f32_16x16x32_bf16 v[30:33], v[54:57], v[74:77], v[30:33]
	s_add_u32 s10, s69, 0x81000
	s_addc_u32 s11, s70, 0
	global_load_dwordx4 v[34:37], v49, s[10:11]
	ds_read_b64_tr_b16 v[54:55], v171 offset:24576
	ds_read_b64_tr_b16 v[56:57], v171 offset:25600
	ds_read_b128 v[66:69], v187
	s_waitcnt lgkmcnt(3)
	v_mfma_f32_16x16x32_bf16 v[10:13], v[58:61], v[74:77], v[10:13]
	global_load_dwordx4 v[22:25], v49, s[10:11] offset:2048
	ds_read_b64_tr_b16 v[58:59], v179 offset:24576
	ds_read_b64_tr_b16 v[60:61], v179 offset:25600
	s_waitcnt lgkmcnt(2)
	v_mfma_f32_16x16x32_bf16 v[94:97], v[54:57], v[66:69], v[42:45]
	s_mov_b32 s48, m0
	s_mov_b32 m0, s46
	s_nop 0
	global_load_lds_dwordx4 v169, s[50:51]
	s_mov_b32 m0, s48
	s_nop 2
	ds_read_b64_tr_b16 v[42:43], v180 offset:24576
	ds_read_b64_tr_b16 v[44:45], v180 offset:25600
	s_waitcnt lgkmcnt(2)
	v_mfma_f32_16x16x32_bf16 v[90:93], v[58:61], v[66:69], v[50:53]
	s_mov_b32 s48, m0
	s_mov_b32 m0, s47
	s_nop 0
	global_load_lds_dwordx4 v170, s[50:51]
	s_mov_b32 m0, s48
	s_nop 2
	ds_read_b64_tr_b16 v[50:51], v181 offset:24576
	ds_read_b64_tr_b16 v[52:53], v181 offset:25600
	s_waitcnt lgkmcnt(2)
	v_mfma_f32_16x16x32_bf16 v[70:73], v[42:45], v[66:69], v[244:247]
	s_nop 2
	ds_read_b64_tr_b16 v[244:245], v182 offset:24576
	ds_read_b64_tr_b16 v[246:247], v182 offset:25600
	s_waitcnt lgkmcnt(2)
	v_mfma_f32_16x16x32_bf16 v[42:45], v[50:53], v[66:69], v[248:251]
	s_nop 2
	ds_read_b64_tr_b16 v[248:249], v183 offset:24576
	ds_read_b64_tr_b16 v[250:251], v183 offset:25600
	s_waitcnt lgkmcnt(2)
	v_mfma_f32_16x16x32_bf16 v[86:89], v[244:247], v[66:69], v[240:243]
	s_nop 2
	ds_read_b64_tr_b16 v[240:241], v184 offset:24576
	ds_read_b64_tr_b16 v[242:243], v184 offset:25600
	s_waitcnt lgkmcnt(2)
	v_mfma_f32_16x16x32_bf16 v[62:65], v[248:251], v[66:69], v[236:239]
	ds_read_b64_tr_b16 v[50:51], v185 offset:24576
	ds_read_b64_tr_b16 v[52:53], v185 offset:25600
	s_waitcnt lgkmcnt(2)
	v_mfma_f32_16x16x32_bf16 v[30:33], v[240:243], v[66:69], v[30:33]
	s_waitcnt lgkmcnt(0)
	v_mfma_f32_16x16x32_bf16 v[10:13], v[50:53], v[66:69], v[10:13]
	s_waitcnt lgkmcnt(0)
	s_barrier
	s_mov_b32 s48, s49
	s_cbranch_vccnz .LBB0_889
	s_waitcnt vmcnt(0)
	s_waitcnt lgkmcnt(0)
	s_barrier
	v_mov_b32_e32 v77, 0
	v_mov_b32_e32 v76, v77
	v_mov_b32_e32 v75, v77
	v_mov_b32_e32 v74, v77
	v_mov_b32_e32 v81, v77
	v_mov_b32_e32 v80, v77
	v_mov_b32_e32 v79, v77
	v_mov_b32_e32 v78, v77
	v_mov_b32_e32 v125, v77
	v_mov_b32_e32 v124, v77
	v_mov_b32_e32 v123, v77
	v_mov_b32_e32 v122, v77
	v_mov_b32_e32 v49, v77
	v_mov_b32_e32 v48, v77
	v_mov_b32_e32 v47, v77
	v_mov_b32_e32 v46, v77
	v_mov_b32_e32 v61, v77
	v_mov_b32_e32 v60, v77
	v_mov_b32_e32 v59, v77
	v_mov_b32_e32 v58, v77
	v_mov_b32_e32 v117, v77
	v_mov_b32_e32 v116, v77
	v_mov_b32_e32 v115, v77
	v_mov_b32_e32 v114, v77
	v_mov_b32_e32 v21, v77
	v_mov_b32_e32 v20, v77
	v_mov_b32_e32 v19, v77
	v_mov_b32_e32 v18, v77
	v_mov_b32_e32 v41, v77
	v_mov_b32_e32 v40, v77
	v_mov_b32_e32 v39, v77
	v_mov_b32_e32 v38, v77
	v_mov_b32_e32 v109, v77
	v_mov_b32_e32 v108, v77
	v_mov_b32_e32 v107, v77
	v_mov_b32_e32 v106, v77
	v_mov_b32_e32 v9, v77
	v_mov_b32_e32 v8, v77
	v_mov_b32_e32 v7, v77
	v_mov_b32_e32 v6, v77
	v_mov_b32_e32 v25, v77
	v_mov_b32_e32 v24, v77
	v_mov_b32_e32 v23, v77
	v_mov_b32_e32 v22, v77
	v_mov_b32_e32 v105, v77
	v_mov_b32_e32 v104, v77
	v_mov_b32_e32 v103, v77
	v_mov_b32_e32 v102, v77
	v_mov_b32_e32 v57, v77
	v_mov_b32_e32 v56, v77
	v_mov_b32_e32 v55, v77
	v_mov_b32_e32 v54, v77
	v_mov_b32_e32 v85, v77
	v_mov_b32_e32 v84, v77
	v_mov_b32_e32 v83, v77
	v_mov_b32_e32 v82, v77
	v_mov_b32_e32 v129, v77
	v_mov_b32_e32 v128, v77
	v_mov_b32_e32 v127, v77
	v_mov_b32_e32 v126, v77
	v_mov_b32_e32 v37, v77
	v_mov_b32_e32 v36, v77
	v_mov_b32_e32 v35, v77
	v_mov_b32_e32 v34, v77
	v_mov_b32_e32 v69, v77
	v_mov_b32_e32 v68, v77
	v_mov_b32_e32 v67, v77
	v_mov_b32_e32 v66, v77
	v_mov_b32_e32 v121, v77
	v_mov_b32_e32 v120, v77
	v_mov_b32_e32 v119, v77
	v_mov_b32_e32 v118, v77
	v_mov_b32_e32 v17, v77
	v_mov_b32_e32 v16, v77
	v_mov_b32_e32 v15, v77
	v_mov_b32_e32 v14, v77
	v_mov_b32_e32 v53, v77
	v_mov_b32_e32 v52, v77
	v_mov_b32_e32 v51, v77
	v_mov_b32_e32 v50, v77
	v_mov_b32_e32 v113, v77
	v_mov_b32_e32 v112, v77
	v_mov_b32_e32 v111, v77
	v_mov_b32_e32 v110, v77
	v_mov_b32_e32 v5, v77
	v_mov_b32_e32 v4, v77
	v_mov_b32_e32 v3, v77
	v_mov_b32_e32 v2, v77
	v_mov_b32_e32 v29, v77
	v_mov_b32_e32 v28, v77
	v_mov_b32_e32 v27, v77
	v_mov_b32_e32 v26, v77
	v_mov_b32_e32 v101, v77
	v_mov_b32_e32 v100, v77
	v_mov_b32_e32 v99, v77
	v_mov_b32_e32 v98, v77
